# diff-attention: K/V LDS-DMA issue moved from the post-barrier block into the stage-2 softmax head (interleaved)
# speedup vs baseline: 1.0098x; 1.0082x over previous
.Lattn_mid:
	s_waitcnt vmcnt(0) lgkmcnt(0)
	s_barrier
	s_cmp_gt_i32 s16, s45
	s_cbranch_scc1 .Lattn_dmaonly
	v_add3_u32 v212, v238, v248, s48
	v_xor_b32_e32 v228, 0x40, v248
	v_add3_u32 v213, v238, v228, s48
	v_xor_b32_e32 v228, 0x80, v248
	v_add3_u32 v214, v238, v228, s48
	v_xor_b32_e32 v228, 0xc0, v248
	v_add3_u32 v215, v238, v228, s48
	s_cmp_eq_u32 s16, s45
	s_cbranch_scc1 .Lattn_s2last
	ds_read_b64_tr_b16 v[176:177], v212 offset:32768
	ds_read_b64_tr_b16 v[178:179], v212 offset:34816
	ds_read_b64_tr_b16 v[180:181], v213 offset:32768
	ds_read_b64_tr_b16 v[182:183], v213 offset:34816
	ds_read_b64_tr_b16 v[184:185], v214 offset:32768
	ds_read_b64_tr_b16 v[186:187], v214 offset:34816
	s_cmpk_gt_i32 s47, 0xff66
	s_cbranch_scc0 .Lattn_nobias1_c
	ds_read2_b32 v[192:193], v250 offset0:0 offset1:1
	ds_read2_b32 v[194:195], v250 offset0:2 offset1:3
	ds_read2_b32 v[196:197], v250 offset0:32 offset1:33
	ds_read2_b32 v[198:199], v250 offset0:34 offset1:35
	ds_read2_b32 v[200:201], v250 offset0:8 offset1:9
	ds_read2_b32 v[202:203], v250 offset0:10 offset1:11
	ds_read2_b32 v[204:205], v250 offset0:40 offset1:41
	ds_read2_b32 v[206:207], v250 offset0:42 offset1:43
	s_waitcnt lgkmcnt(7)
	v_add_f32_e32 v128, v128, v192
	v_add_f32_e32 v129, v129, v193
	s_waitcnt lgkmcnt(6)
	v_add_f32_e32 v130, v130, v194
	v_add_f32_e32 v131, v131, v195
	s_waitcnt lgkmcnt(5)
	v_add_f32_e32 v144, v144, v196
	v_add_f32_e32 v145, v145, v197
	s_waitcnt lgkmcnt(4)
	v_add_f32_e32 v146, v146, v198
	v_add_f32_e32 v147, v147, v199
	s_waitcnt lgkmcnt(3)
	v_add_f32_e32 v132, v132, v200
	v_add_f32_e32 v133, v133, v201
	s_waitcnt lgkmcnt(2)
	v_add_f32_e32 v134, v134, v202
	v_add_f32_e32 v135, v135, v203
	s_waitcnt lgkmcnt(1)
	v_add_f32_e32 v148, v148, v204
	v_add_f32_e32 v149, v149, v205
	s_waitcnt lgkmcnt(0)
	v_add_f32_e32 v150, v150, v206
	v_add_f32_e32 v151, v151, v207
	ds_read2_b32 v[192:193], v250 offset0:16 offset1:17
	ds_read2_b32 v[194:195], v250 offset0:18 offset1:19
	ds_read2_b32 v[196:197], v250 offset0:48 offset1:49
	ds_read2_b32 v[198:199], v250 offset0:50 offset1:51
	ds_read2_b32 v[200:201], v250 offset0:24 offset1:25
	ds_read2_b32 v[202:203], v250 offset0:26 offset1:27
	ds_read2_b32 v[204:205], v250 offset0:56 offset1:57
	ds_read2_b32 v[206:207], v250 offset0:58 offset1:59
	s_waitcnt lgkmcnt(7)
	v_add_f32_e32 v136, v136, v192
	v_add_f32_e32 v137, v137, v193
	s_waitcnt lgkmcnt(6)
	v_add_f32_e32 v138, v138, v194
	v_add_f32_e32 v139, v139, v195
	s_waitcnt lgkmcnt(5)
	v_add_f32_e32 v152, v152, v196
	v_add_f32_e32 v153, v153, v197
	s_waitcnt lgkmcnt(4)
	v_add_f32_e32 v154, v154, v198
	v_add_f32_e32 v155, v155, v199
	s_waitcnt lgkmcnt(3)
	v_add_f32_e32 v140, v140, v200
	v_add_f32_e32 v141, v141, v201
	s_waitcnt lgkmcnt(2)
	v_add_f32_e32 v142, v142, v202
	v_add_f32_e32 v143, v143, v203
	s_waitcnt lgkmcnt(1)
	v_add_f32_e32 v156, v156, v204
	v_add_f32_e32 v157, v157, v205
	s_waitcnt lgkmcnt(0)
	v_add_f32_e32 v158, v158, v206
	v_add_f32_e32 v159, v159, v207
.Lattn_nobias1_c:
	v_max3_f32 v228, v128, v129, v130
	v_max3_f32 v229, v131, v132, v133
	s_waitcnt lgkmcnt(4)
	v_mfma_f32_32x32x16_bf16 v[64:79], v[160:163], v[176:179], v[64:79]
	ds_read_b64_tr_b16 v[188:189], v215 offset:32768
	ds_read_b64_tr_b16 v[190:191], v215 offset:34816
	v_max3_f32 v228, v228, v134, v135
	v_max3_f32 v229, v229, v136, v137
	v_max3_f32 v228, v228, v138, v139
	s_add_i32 s17, s41, 1
	s_cmp_lt_u32 s17, s42
	s_cbranch_scc0 .Lattn_nok0_c
	s_add_u32 s18, s14, 0x68000
	s_addc_u32 s19, s15, 0
	v_lshl_add_u64 v[254:255], v[210:211], 0, s[18:19]
	s_add_i32 s17, s44, s48
	s_mov_b32 m0, s17
	s_nop 0
	global_load_lds_dwordx4 v[254:255], off
.Lattn_nok0_c:
	v_max3_f32 v229, v229, v140, v141
	v_max3_f32 v228, v228, v142, v143
	v_max3_f32 v229, v229, v144, v145
	s_waitcnt lgkmcnt(4)
	v_mfma_f32_32x32x16_bf16 v[32:47], v[160:163], v[180:183], v[32:47]
	ds_read_b64_tr_b16 v[176:177], v212 offset:36864
	ds_read_b64_tr_b16 v[178:179], v212 offset:38912
	v_max3_f32 v228, v228, v146, v147
	v_max3_f32 v229, v229, v148, v149
	s_cmp_lt_u32 s41, s42
	s_cbranch_scc0 .Lattn_nov0_c
	v_lshl_add_u64 v[254:255], v[218:219], 0, s[14:15]
	s_add_i32 s17, s44, s51
	s_add_i32 m0, s17, 0x8000
	s_nop 0
	global_load_lds_dwordx4 v[254:255], off
.Lattn_nov0_c:
	v_max3_f32 v228, v228, v150, v151
	v_max3_f32 v229, v229, v152, v153
	v_max3_f32 v228, v228, v154, v155
	v_max3_f32 v229, v229, v156, v157
	s_waitcnt lgkmcnt(4)
	v_mfma_f32_32x32x16_bf16 v[16:31], v[160:163], v[184:187], v[16:31]
	ds_read_b64_tr_b16 v[180:181], v213 offset:36864
	ds_read_b64_tr_b16 v[182:183], v213 offset:38912
	v_max3_f32 v228, v228, v158, v159
	s_add_i32 s17, s41, 1
	s_cmp_lt_u32 s17, s42
	s_cbranch_scc0 .Lattn_nok1_c
	s_add_u32 s18, s14, 0x68000
	s_addc_u32 s19, s15, 0
	v_lshl_add_u64 v[254:255], v[216:217], 0, s[18:19]
	s_add_i32 s17, s44, s48
	s_add_i32 m0, s17, 0x400
	s_nop 0
	global_load_lds_dwordx4 v[254:255], off
.Lattn_nok1_c:
	v_max_f32_e32 v228, v228, v229
	v_mov_b32_e32 v229, v228
	s_nop 1
	v_permlane32_swap_b32_e32 v228, v229
	v_max_f32_e32 v228, v228, v229
	s_waitcnt lgkmcnt(4)
	v_mfma_f32_32x32x16_bf16 v[0:15], v[160:163], v[188:191], v[0:15]
	ds_read_b64_tr_b16 v[184:185], v214 offset:36864
	ds_read_b64_tr_b16 v[186:187], v214 offset:38912
	s_cmp_lt_u32 s41, s42
	s_cbranch_scc0 .Lattn_nov1_c
	v_lshl_add_u64 v[254:255], v[220:221], 0, s[14:15]
	s_add_i32 s17, s44, s51
	s_add_i32 m0, s17, 0x8400
	s_nop 0
	global_load_lds_dwordx4 v[254:255], off
.Lattn_nov1_c:
	v_add_f32_e32 v228, s49, v228
	v_sub_f32_e32 v229, v228, v227
	v_cmp_lt_f32_e32 vcc, 0x41000000, v229
	s_nop 1
	v_cndmask_b32_e32 v229, v227, v228, vcc
	v_sub_f32_e32 v228, v227, v229
	v_exp_f32_e32 v228, v228
	v_mov_b32_e32 v227, v229
	v_subrev_f32_e32 v229, s49, v229
	v_cmp_neq_f32_e32 vcc, 1.0, v228
	s_cbranch_vccz .Lattn_noresc1_c
	ds_write_b32 v239, v228
	ds_read_b128 v[192:195], v249
	ds_read_b128 v[196:199], v249 offset:32
	ds_read_b128 v[200:203], v249 offset:64
	ds_read_b128 v[204:207], v249 offset:96
	s_waitcnt lgkmcnt(3)
	v_pk_mul_f32 v[112:113], v[112:113], v[192:193]
	v_pk_mul_f32 v[114:115], v[114:115], v[194:195]
	v_pk_mul_f32 v[96:97], v[96:97], v[192:193]
	v_pk_mul_f32 v[98:99], v[98:99], v[194:195]
	v_pk_mul_f32 v[80:81], v[80:81], v[192:193]
	v_pk_mul_f32 v[82:83], v[82:83], v[194:195]
	v_pk_mul_f32 v[48:49], v[48:49], v[192:193]
	v_pk_mul_f32 v[50:51], v[50:51], v[194:195]
	s_waitcnt lgkmcnt(2)
	v_pk_mul_f32 v[116:117], v[116:117], v[196:197]
	v_pk_mul_f32 v[118:119], v[118:119], v[198:199]
	v_pk_mul_f32 v[100:101], v[100:101], v[196:197]
	v_pk_mul_f32 v[102:103], v[102:103], v[198:199]
	v_pk_mul_f32 v[84:85], v[84:85], v[196:197]
	v_pk_mul_f32 v[86:87], v[86:87], v[198:199]
	v_pk_mul_f32 v[52:53], v[52:53], v[196:197]
	v_pk_mul_f32 v[54:55], v[54:55], v[198:199]
	s_waitcnt lgkmcnt(1)
	v_pk_mul_f32 v[120:121], v[120:121], v[200:201]
	v_pk_mul_f32 v[122:123], v[122:123], v[202:203]
	v_pk_mul_f32 v[104:105], v[104:105], v[200:201]
	v_pk_mul_f32 v[106:107], v[106:107], v[202:203]
	v_pk_mul_f32 v[88:89], v[88:89], v[200:201]
	v_pk_mul_f32 v[90:91], v[90:91], v[202:203]
	v_pk_mul_f32 v[56:57], v[56:57], v[200:201]
	v_pk_mul_f32 v[58:59], v[58:59], v[202:203]
	s_waitcnt lgkmcnt(0)
	v_pk_mul_f32 v[124:125], v[124:125], v[204:205]
	v_pk_mul_f32 v[126:127], v[126:127], v[206:207]
	v_pk_mul_f32 v[108:109], v[108:109], v[204:205]
	v_pk_mul_f32 v[110:111], v[110:111], v[206:207]
	v_pk_mul_f32 v[92:93], v[92:93], v[204:205]
	v_pk_mul_f32 v[94:95], v[94:95], v[206:207]
	v_pk_mul_f32 v[60:61], v[60:61], v[204:205]
	v_pk_mul_f32 v[62:63], v[62:63], v[206:207]

.Lattn_noresc1_d:
	ds_read_b64_tr_b16 v[188:189], v215 offset:36864
	ds_read_b64_tr_b16 v[190:191], v215 offset:38912
	ds_read_b64_tr_b16 v[192:193], v212 offset:40960
	ds_read_b64_tr_b16 v[194:195], v212 offset:43008
	ds_read_b64_tr_b16 v[196:197], v213 offset:40960
	ds_read_b64_tr_b16 v[198:199], v213 offset:43008
	ds_read_b64_tr_b16 v[200:201], v214 offset:40960
	ds_read_b64_tr_b16 v[202:203], v214 offset:43008
	v_sub_f32_e32 v128, v128, v229
	v_sub_f32_e32 v129, v129, v229
	v_sub_f32_e32 v130, v130, v229
	s_waitcnt lgkmcnt(12)
	v_mfma_f32_32x32x16_bf16 v[64:79], v[164:167], v[176:179], v[64:79]
	ds_read_b64_tr_b16 v[204:205], v215 offset:40960
	ds_read_b64_tr_b16 v[206:207], v215 offset:43008
	v_sub_f32_e32 v131, v131, v229
	v_exp_f32_e32 v128, v128
	v_exp_f32_e32 v129, v129
	v_exp_f32_e32 v130, v130
	v_exp_f32_e32 v131, v131
	v_add_f32_e32 v254, v128, v129
	v_add_f32_e32 v254, v254, v130
	v_add_f32_e32 v254, v254, v131
	s_waitcnt lgkmcnt(12)
	v_mfma_f32_32x32x16_bf16 v[32:47], v[164:167], v[180:183], v[32:47]
	ds_read_b64_tr_b16 v[176:177], v212 offset:45056
	ds_read_b64_tr_b16 v[178:179], v212 offset:47104
	v_sub_f32_e32 v132, v132, v229
	v_sub_f32_e32 v133, v133, v229
	v_sub_f32_e32 v134, v134, v229
	v_sub_f32_e32 v135, v135, v229
	v_exp_f32_e32 v132, v132
	v_exp_f32_e32 v133, v133
	v_exp_f32_e32 v134, v134
	v_exp_f32_e32 v135, v135
	v_add_f32_e32 v254, v254, v132
	s_waitcnt lgkmcnt(12)
	v_mfma_f32_32x32x16_bf16 v[16:31], v[164:167], v[184:187], v[16:31]
	ds_read_b64_tr_b16 v[180:181], v213 offset:45056
	ds_read_b64_tr_b16 v[182:183], v213 offset:47104
	v_add_f32_e32 v254, v254, v133
	v_add_f32_e32 v254, v254, v134
	v_add_f32_e32 v254, v254, v135
	v_cvt_pk_bf16_f32 v128, v128, v129
	v_cvt_pk_bf16_f32 v129, v130, v131
	v_sub_f32_e32 v136, v136, v229
	v_sub_f32_e32 v137, v137, v229
	v_sub_f32_e32 v138, v138, v229
	v_sub_f32_e32 v139, v139, v229
	s_waitcnt lgkmcnt(12)
	v_mfma_f32_32x32x16_bf16 v[0:15], v[164:167], v[188:191], v[0:15]
	ds_read_b64_tr_b16 v[184:185], v214 offset:45056
	ds_read_b64_tr_b16 v[186:187], v214 offset:47104
	v_exp_f32_e32 v136, v136
	v_exp_f32_e32 v137, v137
	v_exp_f32_e32 v138, v138
	v_exp_f32_e32 v139, v139
	v_add_f32_e32 v254, v254, v136
	v_add_f32_e32 v254, v254, v137
	v_add_f32_e32 v254, v254, v138
	v_add_f32_e32 v254, v254, v139
	v_cvt_pk_bf16_f32 v130, v132, v133
	s_waitcnt lgkmcnt(12)
	v_mfma_f32_32x32x16_bf16 v[64:79], v[168:171], v[192:195], v[64:79]
	ds_read_b64_tr_b16 v[188:189], v215 offset:45056
	ds_read_b64_tr_b16 v[190:191], v215 offset:47104
	v_cvt_pk_bf16_f32 v131, v134, v135
	v_sub_f32_e32 v140, v140, v229
	v_sub_f32_e32 v141, v141, v229
	v_sub_f32_e32 v142, v142, v229
	v_sub_f32_e32 v143, v143, v229
	v_exp_f32_e32 v140, v140
	v_exp_f32_e32 v141, v141
	v_exp_f32_e32 v142, v142
	s_waitcnt lgkmcnt(12)
	v_mfma_f32_32x32x16_bf16 v[32:47], v[168:171], v[196:199], v[32:47]
	v_exp_f32_e32 v143, v143
	v_add_f32_e32 v254, v254, v140
	v_add_f32_e32 v254, v254, v141
	v_add_f32_e32 v254, v254, v142
	v_add_f32_e32 v254, v254, v143
	v_cvt_pk_bf16_f32 v132, v136, v137
	v_cvt_pk_bf16_f32 v133, v138, v139
	v_sub_f32_e32 v144, v144, v229
	v_sub_f32_e32 v145, v145, v229
	s_waitcnt lgkmcnt(10)
	v_mfma_f32_32x32x16_bf16 v[16:31], v[168:171], v[200:203], v[16:31]
	v_sub_f32_e32 v146, v146, v229
	v_sub_f32_e32 v147, v147, v229
	v_exp_f32_e32 v144, v144
	v_exp_f32_e32 v145, v145
	v_exp_f32_e32 v146, v146
	v_exp_f32_e32 v147, v147
	v_add_f32_e32 v255, v144, v145
	v_add_f32_e32 v255, v255, v146
	v_add_f32_e32 v255, v255, v147
	s_waitcnt lgkmcnt(8)
	v_mfma_f32_32x32x16_bf16 v[0:15], v[168:171], v[204:207], v[0:15]
	v_cvt_pk_bf16_f32 v134, v140, v141
	v_cvt_pk_bf16_f32 v135, v142, v143
	v_sub_f32_e32 v148, v148, v229
	v_sub_f32_e32 v149, v149, v229
	v_sub_f32_e32 v150, v150, v229
	v_sub_f32_e32 v151, v151, v229
	v_exp_f32_e32 v148, v148
	v_exp_f32_e32 v149, v149
	v_exp_f32_e32 v150, v150
	s_waitcnt lgkmcnt(6)
	v_mfma_f32_32x32x16_bf16 v[64:79], v[172:175], v[176:179], v[64:79]
	v_exp_f32_e32 v151, v151
	v_add_f32_e32 v255, v255, v148
	v_add_f32_e32 v255, v255, v149
	v_add_f32_e32 v255, v255, v150
	v_add_f32_e32 v255, v255, v151
	v_cvt_pk_bf16_f32 v136, v144, v145
	v_cvt_pk_bf16_f32 v137, v146, v147
	v_sub_f32_e32 v152, v152, v229
	v_sub_f32_e32 v153, v153, v229
	s_waitcnt lgkmcnt(4)
	v_mfma_f32_32x32x16_bf16 v[32:47], v[172:175], v[180:183], v[32:47]
	v_sub_f32_e32 v154, v154, v229
	v_sub_f32_e32 v155, v155, v229
	v_exp_f32_e32 v152, v152
	v_exp_f32_e32 v153, v153
	v_exp_f32_e32 v154, v154
	v_exp_f32_e32 v155, v155
	v_add_f32_e32 v255, v255, v152
	v_add_f32_e32 v255, v255, v153
	s_waitcnt lgkmcnt(2)
	v_mfma_f32_32x32x16_bf16 v[16:31], v[172:175], v[184:187], v[16:31]
	v_add_f32_e32 v255, v255, v154
	v_add_f32_e32 v255, v255, v155
	v_cvt_pk_bf16_f32 v138, v148, v149
	v_cvt_pk_bf16_f32 v139, v150, v151
	v_sub_f32_e32 v156, v156, v229
	v_sub_f32_e32 v157, v157, v229
	v_sub_f32_e32 v158, v158, v229
	v_sub_f32_e32 v159, v159, v229
	v_exp_f32_e32 v156, v156
	s_waitcnt lgkmcnt(0)
	v_mfma_f32_32x32x16_bf16 v[0:15], v[172:175], v[188:191], v[0:15]
	v_exp_f32_e32 v157, v157
	v_exp_f32_e32 v158, v158
	v_exp_f32_e32 v159, v159
	v_add_f32_e32 v255, v255, v156
	v_add_f32_e32 v255, v255, v157
	v_add_f32_e32 v255, v255, v158
	v_add_f32_e32 v255, v255, v159
	v_cvt_pk_bf16_f32 v140, v152, v153
	v_cvt_pk_bf16_f32 v141, v154, v155
	v_cvt_pk_bf16_f32 v142, v156, v157
	v_cvt_pk_bf16_f32 v143, v158, v159
	v_add_f32_e32 v254, v254, v255
	v_mov_b32_e32 v255, v254
	s_nop 1
	v_permlane32_swap_b32_e32 v254, v255
	v_add_f32_e32 v254, v254, v255
	v_fma_f32 v208, v208, v228, v254
	s_branch .Lattn_tail
.Lattn_dmaonly:
	s_add_i32 s17, s41, 1
	s_cmp_lt_u32 s17, s42
	s_cbranch_scc0 .Lattn_nok0_e
	s_add_u32 s18, s14, 0x68000
	s_addc_u32 s19, s15, 0
	v_lshl_add_u64 v[254:255], v[210:211], 0, s[18:19]
	s_add_i32 s17, s44, s48
	s_mov_b32 m0, s17
	s_nop 0
	global_load_lds_dwordx4 v[254:255], off
.Lattn_nok0_e:
	s_cmp_lt_u32 s41, s42
	s_cbranch_scc0 .Lattn_nov0_e
	v_lshl_add_u64 v[254:255], v[218:219], 0, s[14:15]
	s_add_i32 s17, s44, s51
	s_add_i32 m0, s17, 0x8000
	s_nop 0
	global_load_lds_dwordx4 v[254:255], off
.Lattn_nov0_e:
	s_add_i32 s17, s41, 1
	s_cmp_lt_u32 s17, s42
	s_cbranch_scc0 .Lattn_nok1_e
	s_add_u32 s18, s14, 0x68000
	s_addc_u32 s19, s15, 0
	v_lshl_add_u64 v[254:255], v[216:217], 0, s[18:19]
	s_add_i32 s17, s44, s48
	s_add_i32 m0, s17, 0x400
	s_nop 0
	global_load_lds_dwordx4 v[254:255], off
.Lattn_nok1_e:
	s_cmp_lt_u32 s41, s42
	s_cbranch_scc0 .Lattn_nov1_e
	v_lshl_add_u64 v[254:255], v[220:221], 0, s[14:15]
	s_add_i32 s17, s44, s51
	s_add_i32 m0, s17, 0x8400
	s_nop 0
	global_load_lds_dwordx4 v[254:255], off
.Lattn_nov1_e:
.Lattn_tail:
	s_addk_i32 s43, 0x4000
	s_add_i32 s41, s41, 1
	s_add_u32 s14, s14, 0x68000
	s_addc_u32 s15, s15, 0
	s_add_i32 s47, s47, 64
	v_add_u32_e32 v250, 0x100, v250
	s_cmp_lg_u32 s46, s14
	s_cbranch_scc1 .Lattn_loop
	s_add_i32 s17, s45, 1
	s_cmp_eq_u32 s17, s42
	s_cbranch_scc0 .Lattn_done
	ds_read_b64_tr_b16 v[192:193], v212 offset:32768
	ds_read_b64_tr_b16 v[194:195], v212 offset:34816
	ds_read_b64_tr_b16 v[196:197], v213 offset:32768
	ds_read_b64_tr_b16 v[198:199], v213 offset:34816
	ds_read_b64_tr_b16 v[200:201], v214 offset:32768
	ds_read_b64_tr_b16 v[202:203], v214 offset:34816
	ds_read_b64_tr_b16 v[204:205], v215 offset:32768
	ds_read_b64_tr_b16 v[206:207], v215 offset:34816
	ds_read_b64_tr_b16 v[144:145], v212 offset:36864
	ds_read_b64_tr_b16 v[146:147], v212 offset:38912
	ds_read_b64_tr_b16 v[148:149], v213 offset:36864
	ds_read_b64_tr_b16 v[150:151], v213 offset:38912
	ds_read_b64_tr_b16 v[152:153], v214 offset:36864
	ds_read_b64_tr_b16 v[154:155], v214 offset:38912
	s_waitcnt lgkmcnt(12)
	v_mfma_f32_32x32x16_bf16 v[112:127], v[128:131], v[192:195], v[112:127]
	ds_read_b64_tr_b16 v[156:157], v215 offset:36864
	ds_read_b64_tr_b16 v[158:159], v215 offset:38912
	s_waitcnt lgkmcnt(12)
	v_mfma_f32_32x32x16_bf16 v[96:111], v[128:131], v[196:199], v[96:111]
	ds_read_b64_tr_b16 v[160:161], v212 offset:40960
	ds_read_b64_tr_b16 v[162:163], v212 offset:43008
	s_waitcnt lgkmcnt(12)
	v_mfma_f32_32x32x16_bf16 v[80:95], v[128:131], v[200:203], v[80:95]
	ds_read_b64_tr_b16 v[164:165], v213 offset:40960
	ds_read_b64_tr_b16 v[166:167], v213 offset:43008
	s_waitcnt lgkmcnt(12)
	v_mfma_f32_32x32x16_bf16 v[48:63], v[128:131], v[204:207], v[48:63]
	ds_read_b64_tr_b16 v[168:169], v214 offset:40960
	ds_read_b64_tr_b16 v[170:171], v214 offset:43008
	s_waitcnt lgkmcnt(12)
	v_mfma_f32_32x32x16_bf16 v[112:127], v[132:135], v[144:147], v[112:127]
	ds_read_b64_tr_b16 v[172:173], v215 offset:40960
	ds_read_b64_tr_b16 v[174:175], v215 offset:43008
	s_waitcnt lgkmcnt(12)
	v_mfma_f32_32x32x16_bf16 v[96:111], v[132:135], v[148:151], v[96:111]
	ds_read_b64_tr_b16 v[176:177], v212 offset:45056
	ds_read_b64_tr_b16 v[178:179], v212 offset:47104
	s_waitcnt lgkmcnt(12)
	v_mfma_f32_32x32x16_bf16 v[80:95], v[132:135], v[152:155], v[80:95]
	ds_read_b64_tr_b16 v[180:181], v213 offset:45056
	ds_read_b64_tr_b16 v[182:183], v213 offset:47104
	s_waitcnt lgkmcnt(12)
	v_mfma_f32_32x32x16_bf16 v[48:63], v[132:135], v[156:159], v[48:63]
	ds_read_b64_tr_b16 v[184:185], v214 offset:45056
	ds_read_b64_tr_b16 v[186:187], v214 offset:47104
	s_waitcnt lgkmcnt(12)
	v_mfma_f32_32x32x16_bf16 v[112:127], v[136:139], v[160:163], v[112:127]
	ds_read_b64_tr_b16 v[188:189], v215 offset:45056
	ds_read_b64_tr_b16 v[190:191], v215 offset:47104
	s_waitcnt lgkmcnt(12)
	v_mfma_f32_32x32x16_bf16 v[96:111], v[136:139], v[164:167], v[96:111]
	s_waitcnt lgkmcnt(10)
	v_mfma_f32_32x32x16_bf16 v[80:95], v[136:139], v[168:171], v[80:95]
	s_waitcnt lgkmcnt(8)
	v_mfma_f32_32x32x16_bf16 v[48:63], v[136:139], v[172:175], v[48:63]
	s_waitcnt lgkmcnt(6)
	v_mfma_f32_32x32x16_bf16 v[112:127], v[140:143], v[176:179], v[112:127]
	s_waitcnt lgkmcnt(4)
	v_mfma_f32_32x32x16_bf16 v[96:111], v[140:143], v[180:183], v[96:111]
	s_waitcnt lgkmcnt(2)
	v_mfma_f32_32x32x16_bf16 v[80:95], v[140:143], v[184:187], v[80:95]
	s_waitcnt lgkmcnt(0)
	v_mfma_f32_32x32x16_bf16 v[48:63], v[140:143], v[188:191], v[48:63]
